# adds double-buffered q-chunk prefetch in the MoBA block-gating loop on top of the v_rcp_f32 sigmoid epilogues
# speedup vs baseline: 1.0059x; 1.0059x over previous
.LBB0_1350:
	s_or_b64 exec, exec, s[0:1]
	v_cmp_eq_u32_e64 s[36:37], 0, v0
	s_and_saveexec_b64 s[0:1], s[36:37]
	v_mov_b32_e32 v1, s51
	ds_write_b32 v1, v3
	s_or_b64 exec, exec, s[0:1]
	s_mul_i32 s15, s28, 40
	s_and_b32 s29, s73, 15
	s_add_i32 s78, s15, 16
	v_cmp_gt_i32_e32 vcc, s63, v0
	s_waitcnt vmcnt(0) lgkmcnt(0)
	s_barrier
	s_and_saveexec_b64 s[52:53], vcc
	s_cbranch_execz .LBB0_1395
	s_and_b32 s40, s72, 15
	s_cmp_lg_u32 s29, 0
	s_cselect_b64 s[8:9], -1, 0
	s_cmp_gt_u32 s29, 1
	s_cselect_b64 s[66:67], -1, 0
	s_cmp_gt_u32 s29, 2
	s_cselect_b64 s[74:75], -1, 0
	s_cmp_gt_u32 s29, 3
	s_cselect_b64 s[76:77], -1, 0
	s_cmp_gt_u32 s29, 4
	s_cselect_b64 s[82:83], -1, 0
	s_cmp_gt_u32 s29, 5
	s_cselect_b64 s[86:87], -1, 0
	s_cmp_gt_u32 s29, 6
	s_cselect_b64 s[0:1], -1, 0
	s_cmp_gt_u32 s29, 7
	s_cselect_b64 s[70:71], -1, 0
	s_cmp_gt_u32 s29, 8
	s_cselect_b64 s[4:5], -1, 0
	s_cmp_gt_u32 s29, 9
	s_cselect_b64 s[6:7], -1, 0
	s_cmp_gt_u32 s29, 10
	s_cselect_b64 s[92:93], -1, 0
	s_cmp_gt_u32 s29, 11
	s_cselect_b64 s[94:95], -1, 0
	s_cmp_gt_u32 s29, 12
	s_cselect_b64 s[20:21], -1, 0
	s_cmp_gt_u32 s29, 13
	s_cselect_b64 s[2:3], -1, 0
	s_cmp_eq_u32 s29, 15
	s_cselect_b64 s[22:23], -1, 0
	s_add_i32 s38, s78, s30
	s_ashr_i32 s39, s38, 31
	s_lshl_b64 s[38:39], s[38:39], 19
	v_lshl_add_u32 v4, s40, 8, v0
	v_ashrrev_i32_e32 v5, 31, v4
	s_add_u32 s38, s31, s38
	v_lshlrev_b64 v[4:5], 7, v[4:5]
	s_addc_u32 s39, s68, s39
	s_mov_b32 s41, 0
	v_lshl_add_u64 v[4:5], s[38:39], 0, v[4:5]
	v_mov_b32_e32 v1, 0
	v_mov_b32_e32 v2, 0
	v_mov_b32_e32 v14, 0
	v_mov_b32_e32 v15, 0
	v_mov_b32_e32 v17, 0
	v_mov_b32_e32 v18, 0
	v_mov_b32_e32 v19, 0
	v_mov_b32_e32 v20, 0
	v_mov_b32_e32 v21, 0
	v_mov_b32_e32 v22, 0
	v_mov_b32_e32 v23, 0
	v_mov_b32_e32 v24, 0
	v_mov_b32_e32 v25, 0
	v_mov_b32_e32 v26, 0
	v_mov_b32_e32 v27, 0
	global_load_dwordx4 v[176:179], v[4:5], off
	s_branch .LBB0_1355

.LBB0_1355:
	v_cndmask_b32_e64 v6, 0, 1, s[8:9]
	v_cmp_ne_u32_e64 s[38:39], 1, v6
	s_andn2_b64 vcc, exec, s[8:9]
	s_add_i32 s42, s41, 0
	s_waitcnt vmcnt(0)
	v_lshlrev_b32_e32 v12, 16, v176
	v_and_b32_e32 v13, 0xffff0000, v176
	v_lshlrev_b32_e32 v10, 16, v177
	v_and_b32_e32 v11, 0xffff0000, v177
	v_lshlrev_b32_e32 v8, 16, v178
	v_and_b32_e32 v9, 0xffff0000, v178
	v_lshlrev_b32_e32 v6, 16, v179
	v_and_b32_e32 v7, 0xffff0000, v179
	global_load_dwordx4 v[176:179], v[4:5], off offset:16
	s_cbranch_vccnz .LBB0_1357
	s_add_i32 s34, s42, 0x22000
	v_mov_b32_e32 v28, s34
	ds_read_b128 v[28:31], v28
	s_add_i32 s34, s42, 0x22010
	s_waitcnt lgkmcnt(0)
	v_pk_mul_f32 v[28:29], v[28:29], v[12:13]
	s_nop 0
	v_add_f32_e32 v2, v2, v28
	v_add_f32_e32 v2, v2, v29
	v_pk_mul_f32 v[28:29], v[30:31], v[10:11]
	s_nop 0
	v_add_f32_e32 v2, v2, v28
	v_mov_b32_e32 v28, s34
	v_add_f32_e32 v2, v2, v29
	ds_read_b128 v[28:31], v28
	s_waitcnt lgkmcnt(0)
	v_pk_mul_f32 v[28:29], v[28:29], v[8:9]
	s_nop 0
	v_add_f32_e32 v2, v2, v28
	v_add_f32_e32 v2, v2, v29
	v_pk_mul_f32 v[28:29], v[30:31], v[6:7]
	s_nop 0
	v_add_f32_e32 v2, v2, v28
	v_add_f32_e32 v2, v2, v29
